# plus: SwiGLU epilogue of the MoE gate/up GEMM uses v_rcp_f32*x instead of the IEEE division expansion (f32, 1 ulp)
# speedup vs baseline: 1.0071x; 1.0071x over previous
.LBB0_1206:
	v_mul_f32_e32 v0, 0xbfb8aa3b, v188
	v_exp_f32_e32 v0, v0
	v_mul_f32_e32 v5, 0xbfb8aa3b, v189
	v_exp_f32_e32 v5, v5
	s_lshl_b32 s79, s79, 8
	v_add_f32_e32 v0, 1.0, v0
	v_rcp_f32_e32 v2, v0
	s_lshl_b32 s10, s78, 7
	s_add_i32 s11, s79, s66
	v_add_f32_e32 v3, 1.0, v5
	v_rcp_f32_e32 v6, v3
	v_mul_f32_e32 v1, v188, v2
	v_mul_f32_e32 v4, 0xbfb8aa3b, v190
	v_mov_b32_e32 v0, v1
	v_exp_f32_e32 v4, v4
	s_nop 0
	v_add_f32_e32 v4, 1.0, v4
	v_rcp_f32_e32 v7, v4
	v_mul_f32_e32 v1, v189, v6
	v_mul_f32_e32 v6, 0xbfb8aa3b, v191
	v_exp_f32_e32 v6, v6
	s_nop 0
	v_add_f32_e32 v5, 1.0, v6
	v_rcp_f32_e32 v8, v5
	v_mul_f32_e32 v2, v190, v7
	v_mul_f32_e32 v7, 0xbfb8aa3b, v180
	v_exp_f32_e32 v7, v7
	s_nop 0
	v_add_f32_e32 v6, 1.0, v7
	v_rcp_f32_e32 v9, v6
	v_mul_f32_e32 v3, v191, v8
	v_mul_f32_e32 v8, 0xbfb8aa3b, v181
	v_exp_f32_e32 v8, v8
	s_nop 0
	v_add_f32_e32 v7, 1.0, v8
	v_rcp_f32_e32 v10, v7
	v_mul_f32_e32 v4, v180, v9
	v_mul_f32_e32 v9, 0xbfb8aa3b, v182
	v_exp_f32_e32 v9, v9
	s_nop 0
	v_add_f32_e32 v8, 1.0, v9
	v_rcp_f32_e32 v11, v8
	v_mul_f32_e32 v5, v181, v10
	v_mul_f32_e32 v10, 0xbfb8aa3b, v183
	v_exp_f32_e32 v10, v10
	s_nop 0
	v_add_f32_e32 v9, 1.0, v10
	v_rcp_f32_e32 v12, v9
	v_mul_f32_e32 v6, v182, v11
	v_mul_f32_e32 v11, 0xbfb8aa3b, v172
	v_exp_f32_e32 v11, v11
	s_nop 0
	v_add_f32_e32 v10, 1.0, v11
	v_rcp_f32_e32 v13, v10
	v_mul_f32_e32 v7, v183, v12
	v_mul_f32_e32 v12, 0xbfb8aa3b, v173
	v_exp_f32_e32 v12, v12
	s_nop 0
	v_add_f32_e32 v11, 1.0, v12
	v_rcp_f32_e32 v14, v11
	v_mul_f32_e32 v8, v172, v13
	v_mul_f32_e32 v13, 0xbfb8aa3b, v174
	v_exp_f32_e32 v13, v13
	s_nop 0
	v_add_f32_e32 v12, 1.0, v13
	v_rcp_f32_e32 v15, v12
	v_mul_f32_e32 v9, v173, v14
	v_mul_f32_e32 v14, 0xbfb8aa3b, v175
	v_exp_f32_e32 v14, v14
	s_nop 0
	v_add_f32_e32 v13, 1.0, v14
	v_rcp_f32_e32 v16, v13
	v_mul_f32_e32 v10, v174, v15
	v_mul_f32_e32 v15, 0xbfb8aa3b, v164
	v_exp_f32_e32 v15, v15
	s_nop 0
	v_add_f32_e32 v14, 1.0, v15
	v_rcp_f32_e32 v17, v14
	v_mul_f32_e32 v11, v175, v16
	v_mul_f32_e32 v16, 0xbfb8aa3b, v165
	v_exp_f32_e32 v16, v16
	s_nop 0
	v_add_f32_e32 v15, 1.0, v16
	v_rcp_f32_e32 v18, v15
	v_mul_f32_e32 v12, v164, v17
	v_mul_f32_e32 v17, 0xbfb8aa3b, v166
	v_exp_f32_e32 v17, v17
	s_nop 0
	v_add_f32_e32 v16, 1.0, v17
	v_rcp_f32_e32 v19, v16
	v_mul_f32_e32 v13, v165, v18
	v_mul_f32_e32 v18, 0xbfb8aa3b, v167
	v_exp_f32_e32 v18, v18
	s_nop 0
	v_add_f32_e32 v17, 1.0, v18
	v_rcp_f32_e32 v20, v17
	v_mul_f32_e32 v14, v166, v19
	v_mul_f32_e32 v19, 0xbfb8aa3b, v156
	v_exp_f32_e32 v19, v19
	s_nop 0
	v_add_f32_e32 v18, 1.0, v19
	v_rcp_f32_e32 v21, v18
	v_mul_f32_e32 v15, v167, v20
	v_mul_f32_e32 v20, 0xbfb8aa3b, v157
	v_exp_f32_e32 v20, v20
	s_nop 0
	v_add_f32_e32 v19, 1.0, v20
	v_rcp_f32_e32 v22, v19
	v_mul_f32_e32 v16, v156, v21
	v_mul_f32_e32 v21, 0xbfb8aa3b, v158
	v_exp_f32_e32 v21, v21
	s_nop 0
	v_add_f32_e32 v20, 1.0, v21
	v_rcp_f32_e32 v23, v20
	v_mul_f32_e32 v17, v157, v22
	v_mul_f32_e32 v22, 0xbfb8aa3b, v159
	v_exp_f32_e32 v22, v22
	s_nop 0
	v_add_f32_e32 v21, 1.0, v22
	v_rcp_f32_e32 v24, v21
	v_mul_f32_e32 v18, v158, v23
	v_mul_f32_e32 v23, 0xbfb8aa3b, v148
	v_exp_f32_e32 v23, v23
	s_nop 0
	v_add_f32_e32 v22, 1.0, v23
	v_rcp_f32_e32 v25, v22
	v_mul_f32_e32 v19, v159, v24
	v_mul_f32_e32 v24, 0xbfb8aa3b, v149
	v_exp_f32_e32 v24, v24
	s_nop 0
	v_add_f32_e32 v23, 1.0, v24
	v_rcp_f32_e32 v26, v23
	v_mul_f32_e32 v20, v148, v25
	v_mul_f32_e32 v25, 0xbfb8aa3b, v150
	v_exp_f32_e32 v25, v25
	s_nop 0
	v_add_f32_e32 v24, 1.0, v25
	v_rcp_f32_e32 v27, v24
	v_mul_f32_e32 v21, v149, v26
	v_mul_f32_e32 v26, 0xbfb8aa3b, v151
	v_exp_f32_e32 v26, v26
	s_nop 0
	v_add_f32_e32 v25, 1.0, v26
	v_rcp_f32_e32 v28, v25
	v_mul_f32_e32 v22, v150, v27
	v_mul_f32_e32 v27, 0xbfb8aa3b, v140
	v_exp_f32_e32 v27, v27
	s_nop 0
	v_add_f32_e32 v26, 1.0, v27
	v_rcp_f32_e32 v29, v26
	v_mul_f32_e32 v23, v151, v28
	v_mul_f32_e32 v28, 0xbfb8aa3b, v141
	v_exp_f32_e32 v28, v28
	s_nop 0
	v_add_f32_e32 v27, 1.0, v28
	v_rcp_f32_e32 v30, v27
	v_mul_f32_e32 v24, v140, v29
	v_mul_f32_e32 v29, 0xbfb8aa3b, v142
	v_exp_f32_e32 v29, v29
	s_nop 0
	v_add_f32_e32 v28, 1.0, v29
	v_rcp_f32_e32 v31, v28
	v_mul_f32_e32 v25, v141, v30
	v_mul_f32_e32 v30, 0xbfb8aa3b, v143
	v_exp_f32_e32 v30, v30
	s_nop 0
	v_add_f32_e32 v29, 1.0, v30
	v_rcp_f32_e32 v32, v29
	v_mul_f32_e32 v26, v142, v31
	v_mul_f32_e32 v31, 0xbfb8aa3b, v132
	v_exp_f32_e32 v31, v31
	s_nop 0
	v_add_f32_e32 v30, 1.0, v31
	v_rcp_f32_e32 v33, v30
	v_mul_f32_e32 v27, v143, v32
	v_mul_f32_e32 v32, 0xbfb8aa3b, v133
	v_exp_f32_e32 v32, v32
	s_nop 0
	v_add_f32_e32 v31, 1.0, v32
	v_rcp_f32_e32 v34, v31
	v_mul_f32_e32 v28, v132, v33
	v_mul_f32_e32 v33, 0xbfb8aa3b, v134
	v_exp_f32_e32 v33, v33
	s_nop 0
	v_add_f32_e32 v32, 1.0, v33
	v_rcp_f32_e32 v35, v32
	v_mul_f32_e32 v29, v133, v34
	v_mul_f32_e32 v34, 0xbfb8aa3b, v135
	v_exp_f32_e32 v34, v34
	s_nop 0
	v_add_f32_e32 v33, 1.0, v34
	v_rcp_f32_e32 v36, v33
	v_mul_f32_e32 v30, v134, v35
	v_mul_f32_e32 v35, 0xbfb8aa3b, v124
	v_exp_f32_e32 v35, v35
	s_nop 0
	v_add_f32_e32 v34, 1.0, v35
	v_rcp_f32_e32 v37, v34
	v_mul_f32_e32 v31, v135, v36
	v_mul_f32_e32 v36, 0xbfb8aa3b, v125
	v_exp_f32_e32 v36, v36
	s_nop 0
	v_add_f32_e32 v35, 1.0, v36
	v_rcp_f32_e32 v38, v35
	v_mul_f32_e32 v32, v124, v37
	v_mul_f32_e32 v37, 0xbfb8aa3b, v126
	v_exp_f32_e32 v37, v37
	s_nop 0
	v_add_f32_e32 v36, 1.0, v37
	v_rcp_f32_e32 v39, v36
	v_mul_f32_e32 v33, v125, v38
	v_mul_f32_e32 v38, 0xbfb8aa3b, v127
	v_exp_f32_e32 v38, v38
	s_nop 0
	v_add_f32_e32 v37, 1.0, v38
	v_rcp_f32_e32 v40, v37
	v_mul_f32_e32 v34, v126, v39
	v_mul_f32_e32 v39, 0xbfb8aa3b, v116
	v_exp_f32_e32 v39, v39
	s_nop 0
	v_add_f32_e32 v38, 1.0, v39
	v_rcp_f32_e32 v41, v38
	v_mul_f32_e32 v35, v127, v40
	v_mul_f32_e32 v40, 0xbfb8aa3b, v117
	v_exp_f32_e32 v40, v40
	s_nop 0
	v_add_f32_e32 v39, 1.0, v40
	v_rcp_f32_e32 v42, v39
	v_mul_f32_e32 v36, v116, v41
	v_mul_f32_e32 v41, 0xbfb8aa3b, v118
	v_exp_f32_e32 v41, v41
	s_nop 0
	v_add_f32_e32 v40, 1.0, v41
	v_rcp_f32_e32 v43, v40
	v_mul_f32_e32 v37, v117, v42
	v_mul_f32_e32 v42, 0xbfb8aa3b, v119
	v_exp_f32_e32 v42, v42
	s_nop 0
	v_add_f32_e32 v41, 1.0, v42
	v_rcp_f32_e32 v44, v41
	v_mul_f32_e32 v38, v118, v43
	v_mul_f32_e32 v43, 0xbfb8aa3b, v108
	v_exp_f32_e32 v43, v43
	s_nop 0
	v_add_f32_e32 v42, 1.0, v43
	v_rcp_f32_e32 v45, v42
	v_mul_f32_e32 v39, v119, v44
	v_mul_f32_e32 v44, 0xbfb8aa3b, v109
	v_exp_f32_e32 v44, v44
	s_nop 0
	v_add_f32_e32 v43, 1.0, v44
	v_rcp_f32_e32 v46, v43
	v_mul_f32_e32 v40, v108, v45
	v_mul_f32_e32 v45, 0xbfb8aa3b, v110
	v_exp_f32_e32 v45, v45
	s_nop 0
	v_add_f32_e32 v44, 1.0, v45
	v_rcp_f32_e32 v47, v44
	v_mul_f32_e32 v41, v109, v46
	v_mul_f32_e32 v46, 0xbfb8aa3b, v111
	v_exp_f32_e32 v46, v46
	s_nop 0
	v_add_f32_e32 v45, 1.0, v46
	v_rcp_f32_e32 v48, v45
	v_mul_f32_e32 v42, v110, v47
	v_mul_f32_e32 v47, 0xbfb8aa3b, v100
	v_exp_f32_e32 v47, v47
	s_nop 0
	v_add_f32_e32 v46, 1.0, v47
	v_rcp_f32_e32 v49, v46
	v_mul_f32_e32 v43, v111, v48
	v_mul_f32_e32 v48, 0xbfb8aa3b, v101
	v_exp_f32_e32 v48, v48
	s_nop 0
	v_add_f32_e32 v47, 1.0, v48
	v_rcp_f32_e32 v50, v47
	v_mul_f32_e32 v44, v100, v49
	v_mul_f32_e32 v49, 0xbfb8aa3b, v102
	v_exp_f32_e32 v49, v49
	s_nop 0
	v_add_f32_e32 v48, 1.0, v49
	v_rcp_f32_e32 v51, v48
	v_mul_f32_e32 v45, v101, v50
	v_mul_f32_e32 v50, 0xbfb8aa3b, v103
	v_exp_f32_e32 v50, v50
	s_nop 0
	v_add_f32_e32 v49, 1.0, v50
	v_rcp_f32_e32 v52, v49
	v_mul_f32_e32 v46, v102, v51
	v_mul_f32_e32 v51, 0xbfb8aa3b, v92
	v_exp_f32_e32 v51, v51
	s_nop 0
	v_add_f32_e32 v50, 1.0, v51
	v_rcp_f32_e32 v53, v50
	v_mul_f32_e32 v47, v103, v52
	v_mul_f32_e32 v52, 0xbfb8aa3b, v93
	v_exp_f32_e32 v52, v52
	s_nop 0
	v_add_f32_e32 v51, 1.0, v52
	v_rcp_f32_e32 v54, v51
	v_mul_f32_e32 v48, v92, v53
	v_mul_f32_e32 v50, 0xbfb8aa3b, v94
	v_mul_f32_e32 v55, v48, v88
	v_exp_f32_e32 v50, v50
	s_nop 0
	v_add_f32_e32 v50, 1.0, v50
	v_rcp_f32_e32 v53, v50
	v_mul_f32_e32 v48, v93, v54
	v_mul_f32_e32 v51, 0xbfb8aa3b, v95
	v_mul_f32_e32 v54, v48, v89
	v_exp_f32_e32 v51, v51
	s_nop 0
	v_add_f32_e32 v51, 1.0, v51
	v_rcp_f32_e32 v56, v51
	v_mul_f32_e32 v48, v94, v53
	v_mul_f32_e32 v50, 0xbfb8aa3b, v84
	v_mul_f32_e32 v57, v48, v90
	v_exp_f32_e32 v50, v50
	s_nop 0
	v_add_f32_e32 v50, 1.0, v50
	v_rcp_f32_e32 v53, v50
	v_mul_f32_e32 v48, v95, v56
	v_mul_f32_e32 v51, 0xbfb8aa3b, v85
	v_mul_f32_e32 v56, v48, v91
	v_exp_f32_e32 v51, v51
	s_nop 0
	v_add_f32_e32 v51, 1.0, v51
	v_rcp_f32_e32 v58, v51
	v_mul_f32_e32 v48, v84, v53
	v_mul_f32_e32 v50, 0xbfb8aa3b, v86
	v_mul_f32_e32 v59, v48, v80
	v_exp_f32_e32 v50, v50
	s_nop 0
	v_add_f32_e32 v50, 1.0, v50
	v_rcp_f32_e32 v53, v50
	v_mul_f32_e32 v48, v85, v58
	v_mul_f32_e32 v51, 0xbfb8aa3b, v87
	v_mul_f32_e32 v58, v48, v81
	v_exp_f32_e32 v51, v51
	s_nop 0
	v_add_f32_e32 v51, 1.0, v51
	v_rcp_f32_e32 v60, v51
	v_mul_f32_e32 v48, v86, v53
	v_mul_f32_e32 v50, 0xbfb8aa3b, v76
	v_mul_f32_e32 v61, v48, v82
	v_exp_f32_e32 v50, v50
	s_nop 0
	v_add_f32_e32 v50, 1.0, v50
	v_rcp_f32_e32 v53, v50
	v_mul_f32_e32 v48, v87, v60
	v_mul_f32_e32 v51, 0xbfb8aa3b, v77
	v_mul_f32_e32 v60, v48, v83
	v_exp_f32_e32 v51, v51
	s_nop 0
	v_add_f32_e32 v51, 1.0, v51
	v_rcp_f32_e32 v62, v51
	v_mul_f32_e32 v48, v76, v53
	v_mul_f32_e32 v50, 0xbfb8aa3b, v78
	v_mul_f32_e32 v63, v48, v72
	v_exp_f32_e32 v50, v50
	s_nop 0
	v_add_f32_e32 v50, 1.0, v50
	v_rcp_f32_e32 v53, v50
	v_mul_f32_e32 v48, v77, v62
	v_mul_f32_e32 v51, 0xbfb8aa3b, v79
	v_mul_f32_e32 v62, v48, v73
	v_exp_f32_e32 v51, v51
	s_nop 0
	v_add_f32_e32 v51, 1.0, v51
	v_rcp_f32_e32 v72, v51
	v_mul_f32_e32 v48, v78, v53
	v_mul_f32_e32 v50, 0xbfb8aa3b, v68
	v_mul_f32_e32 v73, v48, v74
	v_exp_f32_e32 v50, v50
	s_nop 0
	v_add_f32_e32 v50, 1.0, v50
	v_rcp_f32_e32 v53, v50
	v_mul_f32_e32 v48, v79, v72
	v_mul_f32_e32 v51, 0xbfb8aa3b, v69
	v_mul_f32_e32 v72, v48, v75
	v_exp_f32_e32 v51, v51
	s_nop 0
	v_add_f32_e32 v51, 1.0, v51
	v_rcp_f32_e32 v74, v51
	v_mul_f32_e32 v48, v68, v53
	v_mul_f32_e32 v50, 0xbfb8aa3b, v70
	v_mul_f32_e32 v64, v48, v64
	v_exp_f32_e32 v50, v50
	s_nop 0
	v_add_f32_e32 v50, 1.0, v50
	v_rcp_f32_e32 v53, v50
	v_mul_f32_e32 v48, v69, v74
	v_mul_f32_e32 v51, 0xbfb8aa3b, v71
	v_mul_f32_e32 v65, v48, v65
	v_exp_f32_e32 v51, v51
	s_nop 0
	v_add_f32_e32 v51, 1.0, v51
	v_rcp_f32_e32 v68, v51
	v_mul_f32_e32 v48, v70, v53
	v_mul_f32_e32 v66, v48, v66
	v_mul_f32_e32 v0, v0, v184
	v_mul_f32_e32 v1, v1, v185
	v_mov_b32_e32 v52, 0
	v_cvt_pk_fp8_f32 v52, v0, v1
	v_mul_f32_e32 v2, v2, v186
	v_mul_f32_e32 v3, v3, v187
	v_mul_f32_e32 v8, v8, v168
	v_mul_f32_e32 v9, v9, v169
	v_mul_f32_e32 v12, v12, v160
	v_mul_f32_e32 v13, v13, v161
	v_cvt_pk_fp8_f32 v52, v2, v3 op_sel:[0,0,1]
	v_mov_b32_e32 v2, 0
	v_mov_b32_e32 v3, 0
	v_mul_f32_e32 v48, v71, v68
	v_cvt_pk_fp8_f32 v2, v8, v9
	v_cvt_pk_fp8_f32 v3, v12, v13
	v_mul_f32_e32 v4, v4, v176
	v_mul_f32_e32 v5, v5, v177
	v_mul_f32_e32 v67, v48, v67
	v_mbcnt_lo_u32_b32 v49, -1, 0
	v_mbcnt_hi_u32_b32 v49, -1, v49
	v_mov_b32_e32 v53, 0
	v_and_or_b32 v48, v49, 15, s11
	v_mul_f32_e32 v10, v10, v170
	v_mul_f32_e32 v11, v11, v171
	v_mul_f32_e32 v14, v14, v162
	v_mul_f32_e32 v15, v15, v163
	v_ashrrev_i32_e32 v49, 1, v49
	v_cvt_pk_fp8_f32 v53, v4, v5
	v_or_b32_e32 v4, 16, v48
	s_or_b32 s10, s10, s67
	v_and_b32_e32 v49, -8, v49
	v_ashrrev_i32_e32 v5, 31, v4
	v_cvt_pk_fp8_f32 v2, v10, v11 op_sel:[0,0,1]
	v_cvt_pk_fp8_f32 v3, v14, v15 op_sel:[0,0,1]
	v_add_u32_e32 v50, s10, v49
	v_lshlrev_b64 v[4:5], 10, v[4:5]
	v_ashrrev_i32_e32 v51, 31, v50
	v_lshl_add_u64 v[4:5], s[18:19], 0, v[4:5]
	v_lshl_add_u64 v[4:5], v[4:5], 0, v[50:51]
	v_mul_f32_e32 v16, v16, v152
	v_mul_f32_e32 v17, v17, v153
	v_mul_f32_e32 v20, v20, v144
	v_mul_f32_e32 v21, v21, v145
	global_store_dwordx2 v[4:5], v[2:3], off
	v_mov_b32_e32 v2, 0
	v_mov_b32_e32 v3, 0
	v_cvt_pk_fp8_f32 v2, v16, v17
	v_cvt_pk_fp8_f32 v3, v20, v21
	v_mul_f32_e32 v18, v18, v154
	v_mul_f32_e32 v19, v19, v155
	v_mul_f32_e32 v22, v22, v146
	v_mul_f32_e32 v23, v23, v147
	v_or_b32_e32 v4, 32, v48
	v_ashrrev_i32_e32 v5, 31, v4
	v_cvt_pk_fp8_f32 v2, v18, v19 op_sel:[0,0,1]
	v_cvt_pk_fp8_f32 v3, v22, v23 op_sel:[0,0,1]
	v_lshlrev_b64 v[4:5], 10, v[4:5]
	v_lshl_add_u64 v[4:5], s[18:19], 0, v[4:5]
	v_lshl_add_u64 v[4:5], v[4:5], 0, v[50:51]
	v_mul_f32_e32 v24, v24, v136
	v_mul_f32_e32 v25, v25, v137
	v_mul_f32_e32 v28, v28, v128
	v_mul_f32_e32 v29, v29, v129
	global_store_dwordx2 v[4:5], v[2:3], off
	v_mov_b32_e32 v4, 0
	v_mov_b32_e32 v5, 0
	v_cvt_pk_fp8_f32 v4, v24, v25
	v_cvt_pk_fp8_f32 v5, v28, v29
	v_mul_f32_e32 v26, v26, v138
	v_mul_f32_e32 v27, v27, v139
	v_mul_f32_e32 v30, v30, v130
	v_mul_f32_e32 v31, v31, v131
	v_or_b32_e32 v2, 48, v48
	v_ashrrev_i32_e32 v3, 31, v2
	v_cvt_pk_fp8_f32 v4, v26, v27 op_sel:[0,0,1]
	v_cvt_pk_fp8_f32 v5, v30, v31 op_sel:[0,0,1]
	v_mul_f32_e32 v6, v6, v178
	v_mul_f32_e32 v7, v7, v179
	v_lshlrev_b64 v[2:3], 10, v[2:3]
	v_mul_f32_e32 v32, v32, v120
	v_mul_f32_e32 v33, v33, v121
	v_mul_f32_e32 v36, v36, v112
	v_mul_f32_e32 v37, v37, v113
	v_cvt_pk_fp8_f32 v53, v6, v7 op_sel:[0,0,1]
	v_lshl_add_u64 v[2:3], s[18:19], 0, v[2:3]
	v_mov_b32_e32 v6, 0
	v_mov_b32_e32 v7, 0
	v_cvt_pk_fp8_f32 v6, v32, v33
	v_cvt_pk_fp8_f32 v7, v36, v37
	v_lshl_add_u64 v[2:3], v[2:3], 0, v[50:51]
	v_mul_f32_e32 v40, v40, v104
	v_mul_f32_e32 v41, v41, v105
	v_mul_f32_e32 v44, v44, v96
	v_mul_f32_e32 v45, v45, v97
	global_store_dwordx2 v[2:3], v[4:5], off
	v_mov_b32_e32 v2, 0
	v_mov_b32_e32 v3, 0
	v_ashrrev_i32_e32 v49, 31, v48
	v_cvt_pk_fp8_f32 v2, v40, v41
	v_cvt_pk_fp8_f32 v3, v44, v45
	v_mul_f32_e32 v34, v34, v122
	v_mul_f32_e32 v35, v35, v123
	v_mul_f32_e32 v38, v38, v114
	v_mul_f32_e32 v39, v39, v115
	v_lshlrev_b64 v[0:1], 10, v[48:49]
	v_lshl_add_u64 v[0:1], s[18:19], 0, v[0:1]
	v_cvt_pk_fp8_f32 v6, v34, v35 op_sel:[0,0,1]
	v_cvt_pk_fp8_f32 v7, v38, v39 op_sel:[0,0,1]
	v_mul_f32_e32 v42, v42, v106
	v_mul_f32_e32 v43, v43, v107
	v_mul_f32_e32 v46, v46, v98
	v_mul_f32_e32 v47, v47, v99
	v_lshl_add_u64 v[0:1], v[0:1], 0, v[50:51]
	v_add_co_u32_e32 v4, vcc, s7, v0
	v_cvt_pk_fp8_f32 v2, v42, v43 op_sel:[0,0,1]
	v_cvt_pk_fp8_f32 v3, v46, v47 op_sel:[0,0,1]
	v_addc_co_u32_e32 v5, vcc, 0, v1, vcc
	global_store_dwordx2 v[4:5], v[6:7], off
	v_add_co_u32_e32 v6, vcc, s72, v0
	v_mov_b32_e32 v4, 0
	s_nop 0
	v_addc_co_u32_e32 v7, vcc, 0, v1, vcc
	v_mov_b32_e32 v5, 0
	global_store_dwordx2 v[6:7], v[2:3], off
	v_mov_b32_e32 v6, 0
	v_mov_b32_e32 v7, 0
	v_cvt_pk_fp8_f32 v4, v55, v54
	v_cvt_pk_fp8_f32 v5, v59, v58
	v_cvt_pk_fp8_f32 v6, v63, v62
	v_cvt_pk_fp8_f32 v7, v64, v65
	v_add_co_u32_e32 v2, vcc, s73, v0
	v_cvt_pk_fp8_f32 v4, v57, v56 op_sel:[0,0,1]
	v_cvt_pk_fp8_f32 v5, v61, v60 op_sel:[0,0,1]
	v_addc_co_u32_e32 v3, vcc, 0, v1, vcc
	v_cvt_pk_fp8_f32 v6, v73, v72 op_sel:[0,0,1]
	v_cvt_pk_fp8_f32 v7, v66, v67 op_sel:[0,0,1]
	global_store_dwordx2 v[0:1], v[52:53], off
	v_add_co_u32_e32 v0, vcc, 0x2c000, v0
	s_mov_b64 s[10:11], -1
	s_nop 0
	v_addc_co_u32_e32 v1, vcc, 0, v1, vcc
	s_andn2_b64 vcc, exec, s[22:23]
	global_store_dwordx2 v[2:3], v[4:5], off
	global_store_dwordx2 v[0:1], v[6:7], off
	s_cbranch_vccnz .LBB0_1193
	s_andn2_b64 vcc, exec, s[16:17]
	s_cbranch_vccnz .LBB0_1192
	s_barrier
	s_branch .LBB0_1192
